# speedup vs baseline: 1.0071x; 1.0007x over previous
_Z13gather_kernelPK15HIP_vector_typeIjLj2EEPKiPK6OvfRecPKDF16_PKfPDF16_:
	s_lshr_b32 s3, s2, 2
	s_and_b32 s3, s3, 0x3ffffffe
	s_and_b32 s4, s2, 1
	s_or_b32 s3, s3, s4
	s_cmpk_gt_u32 s3, 0x186
	s_cbranch_scc1 .LBB1_156
	s_load_dwordx4 s[8:11], s[0:1], 0x0
	s_load_dwordx2 s[64:65], s[0:1], 0x20
	s_movk_i32 s4, 0x80
	s_lshl_b32 s12, s3, 4
	s_addk_i32 s12, 0x800
	v_lshrrev_b32_e32 v2, 6, v0
	v_cmp_gt_u32_e64 s[4:5], s4, v0
	v_lshlrev_b32_e32 v1, 2, v0
	v_readfirstlane_b32 s62, v2
	s_and_saveexec_b64 s[6:7], s[4:5]
	v_mov_b32_e32 v2, 0
	ds_write_b32 v1, v2 offset:10832
	s_or_b64 exec, exec, s[6:7]
	s_waitcnt lgkmcnt(0)
	v_cmp_gt_u32_e64 s[6:7], 64, v0
	s_and_saveexec_b64 s[12:13], s[6:7]
	v_mov_b32_e32 v2, 0
	ds_write_b32 v1, v2 offset:11856
	s_or_b64 exec, exec, s[12:13]
	s_mul_i32 s15, s3, 0x5000
	s_mul_hi_u32 s13, s3, 0x5000
	s_add_u32 s8, s8, s15
	s_addc_u32 s9, s9, s13
	v_lshlrev_b32_e32 v2, 3, v0
	v_mov_b32_e32 v3, 0
	v_lshl_add_u64 v[4:5], s[8:9], 0, v[2:3]
	s_movk_i32 s13, 0x1000
	global_load_dwordx2 v[20:21], v2, s[8:9]
	global_load_dwordx2 v[18:19], v2, s[8:9] offset:2048
	v_add_co_u32_e32 v2, vcc, s13, v4
	s_movk_i32 s13, 0x2000
	s_nop 0
	v_addc_co_u32_e32 v3, vcc, 0, v5, vcc
	v_add_co_u32_e32 v6, vcc, s13, v4
	s_movk_i32 s13, 0x3000
	s_nop 0
	v_addc_co_u32_e32 v7, vcc, 0, v5, vcc
	v_add_co_u32_e32 v24, vcc, s13, v4
	v_or_b32_e32 v23, 0x400, v0
	s_nop 0
	v_addc_co_u32_e32 v25, vcc, 0, v5, vcc
	v_lshlrev_b32_e32 v8, 3, v23
	v_or_b32_e32 v22, 0x800, v0
	v_add_co_u32_e32 v26, vcc, 0x4000, v4
	global_load_dwordx2 v[16:17], v[2:3], off
	global_load_dwordx2 v[14:15], v[2:3], off offset:2048
	global_load_dwordx2 v[12:13], v8, s[8:9]
	global_load_dwordx2 v[10:11], v[6:7], off offset:2048
	v_lshlrev_b32_e32 v28, 3, v22
	v_addc_co_u32_e32 v27, vcc, 0, v5, vcc
	global_load_dwordx2 v[8:9], v[24:25], off
	global_load_dwordx2 v[6:7], v[24:25], off offset:2048
	global_load_dwordx2 v[4:5], v28, s[8:9]
	global_load_dwordx2 v[2:3], v[26:27], off offset:2048
	s_lshl_b32 s51, s3, 4
	s_addk_i32 s51, 0x800
	s_load_dwordx4 s[36:39], s[10:11], s51 offset:0x0
	s_load_dword s33, s[10:11], 0x640
	s_load_dword s63, s[64:65], 0x0
	v_mov_b32_e32 v54, 1
	s_waitcnt lgkmcnt(0)
	s_barrier
	s_min_u32 s36, s36, 0x280
	s_min_u32 s37, s37, 0x280
	s_min_u32 s38, s38, 0x280
	s_min_u32 s39, s39, 0x280
	s_addk_i32 s37, 0x280
	s_addk_i32 s38, 0x500
	s_addk_i32 s39, 0x780
	s_cmp_ge_u32 s62, 2
	s_cselect_b32 s54, s37, s36
	s_cselect_b32 s59, s39, s38
	s_mov_b32 s52, s36
	s_mov_b32 s53, s36
	s_mov_b32 s55, s37
	s_mov_b32 s56, s37
	s_mov_b32 s57, s38
	s_mov_b32 s58, s38
	s_mov_b32 s60, s39
	s_mov_b32 s61, s39
	v_cmp_gt_i32_e32 vcc, s52, v0
	s_and_saveexec_b64 s[8:9], vcc
	s_waitcnt vmcnt(9)
	v_lshrrev_b32_e32 v33, 16, v20
	v_lshlrev_b32_e32 v53, 2, v33
	ds_add_rtn_u32 v43, v53, v54 offset:10832
	s_or_b64 exec, exec, s[8:9]
	v_or_b32_e32 v55, 0x100, v0
	v_cmp_gt_i32_e32 vcc, s53, v55
	s_and_saveexec_b64 s[8:9], vcc
	s_waitcnt vmcnt(8)
	v_lshrrev_b32_e32 v34, 16, v18
	v_lshlrev_b32_e32 v53, 2, v34
	ds_add_rtn_u32 v44, v53, v54 offset:10832
	s_or_b64 exec, exec, s[8:9]
	v_or_b32_e32 v55, 0x200, v0
	v_cmp_gt_i32_e32 vcc, s54, v55
	s_and_saveexec_b64 s[8:9], vcc
	s_waitcnt vmcnt(7)
	v_lshrrev_b32_e32 v35, 16, v16
	v_lshlrev_b32_e32 v53, 2, v35
	ds_add_rtn_u32 v45, v53, v54 offset:10832
	s_or_b64 exec, exec, s[8:9]
	v_or_b32_e32 v55, 0x300, v0
	v_cmp_gt_i32_e32 vcc, s55, v55
	s_and_saveexec_b64 s[8:9], vcc
	s_waitcnt vmcnt(6)
	v_lshrrev_b32_e32 v36, 16, v14
	v_lshlrev_b32_e32 v53, 2, v36
	ds_add_rtn_u32 v46, v53, v54 offset:10832
	s_or_b64 exec, exec, s[8:9]
	v_or_b32_e32 v55, 0x400, v0
	v_cmp_gt_i32_e32 vcc, s56, v55
	s_and_saveexec_b64 s[8:9], vcc
	s_waitcnt vmcnt(5)
	v_lshrrev_b32_e32 v37, 16, v12
	v_lshlrev_b32_e32 v53, 2, v37
	ds_add_rtn_u32 v47, v53, v54 offset:10832
	s_or_b64 exec, exec, s[8:9]
	v_or_b32_e32 v55, 0x500, v0
	v_cmp_gt_i32_e32 vcc, s57, v55
	s_and_saveexec_b64 s[8:9], vcc
	s_waitcnt vmcnt(4)
	v_lshrrev_b32_e32 v38, 16, v10
	v_lshlrev_b32_e32 v53, 2, v38
	ds_add_rtn_u32 v48, v53, v54 offset:10832
	s_or_b64 exec, exec, s[8:9]
	v_or_b32_e32 v55, 0x600, v0
	v_cmp_gt_i32_e32 vcc, s58, v55
	s_and_saveexec_b64 s[8:9], vcc
	s_waitcnt vmcnt(3)
	v_lshrrev_b32_e32 v39, 16, v8
	v_lshlrev_b32_e32 v53, 2, v39
	ds_add_rtn_u32 v49, v53, v54 offset:10832
	s_or_b64 exec, exec, s[8:9]
	v_or_b32_e32 v55, 0x700, v0
	v_cmp_gt_i32_e32 vcc, s59, v55
	s_and_saveexec_b64 s[8:9], vcc
	s_waitcnt vmcnt(2)
	v_lshrrev_b32_e32 v40, 16, v6
	v_lshlrev_b32_e32 v53, 2, v40
	ds_add_rtn_u32 v50, v53, v54 offset:10832
	s_or_b64 exec, exec, s[8:9]
	v_or_b32_e32 v55, 0x800, v0
	v_cmp_gt_i32_e32 vcc, s60, v55
	s_and_saveexec_b64 s[8:9], vcc
	s_waitcnt vmcnt(1)
	v_lshrrev_b32_e32 v41, 16, v4
	v_lshlrev_b32_e32 v53, 2, v41
	ds_add_rtn_u32 v51, v53, v54 offset:10832
	s_or_b64 exec, exec, s[8:9]
	v_or_b32_e32 v55, 0x900, v0
	v_cmp_gt_i32_e32 vcc, s61, v55
	s_and_saveexec_b64 s[8:9], vcc
	s_waitcnt vmcnt(0)
	v_lshrrev_b32_e32 v42, 16, v2
	v_lshlrev_b32_e32 v53, 2, v42
	ds_add_rtn_u32 v52, v53, v54 offset:10832
	s_or_b64 exec, exec, s[8:9]
	s_waitcnt lgkmcnt(0)
	v_cmp_gt_i32_e32 vcc, s52, v0
	v_lshl_or_b32 v56, v43, 8, v33
	s_nop 0
	v_cndmask_b32_e32 v32, -1, v56, vcc
	v_or_b32_e32 v55, 0x100, v0
	v_cmp_gt_i32_e32 vcc, s53, v55
	v_lshl_or_b32 v56, v44, 8, v34
	s_nop 0
	v_cndmask_b32_e32 v27, -1, v56, vcc
	v_or_b32_e32 v55, 0x200, v0
	v_cmp_gt_i32_e32 vcc, s54, v55
	v_lshl_or_b32 v56, v45, 8, v35
	s_nop 0
	v_cndmask_b32_e32 v31, -1, v56, vcc
	v_or_b32_e32 v55, 0x300, v0
	v_cmp_gt_i32_e32 vcc, s55, v55
	v_lshl_or_b32 v56, v46, 8, v36
	s_nop 0
	v_cndmask_b32_e32 v26, -1, v56, vcc
	v_or_b32_e32 v55, 0x400, v0
	v_cmp_gt_i32_e32 vcc, s56, v55
	v_lshl_or_b32 v56, v47, 8, v37
	s_nop 0
	v_cndmask_b32_e32 v30, -1, v56, vcc
	v_or_b32_e32 v55, 0x500, v0
	v_cmp_gt_i32_e32 vcc, s57, v55
	v_lshl_or_b32 v56, v48, 8, v38
	s_nop 0
	v_cndmask_b32_e32 v24, -1, v56, vcc
	v_or_b32_e32 v55, 0x600, v0
	v_cmp_gt_i32_e32 vcc, s58, v55
	v_lshl_or_b32 v56, v49, 8, v39
	s_nop 0
	v_cndmask_b32_e32 v29, -1, v56, vcc
	v_or_b32_e32 v55, 0x700, v0
	v_cmp_gt_i32_e32 vcc, s59, v55
	v_lshl_or_b32 v56, v50, 8, v40
	s_nop 0
	v_cndmask_b32_e32 v23, -1, v56, vcc
	v_or_b32_e32 v55, 0x800, v0
	v_cmp_gt_i32_e32 vcc, s60, v55
	v_lshl_or_b32 v56, v51, 8, v41
	s_nop 0
	v_cndmask_b32_e32 v28, -1, v56, vcc
	v_or_b32_e32 v55, 0x900, v0
	v_cmp_gt_i32_e32 vcc, s61, v55
	v_lshl_or_b32 v56, v52, 8, v42
	s_nop 0
	v_cndmask_b32_e32 v22, -1, v56, vcc
